# final6 + per-wave software pipeline v2 in diff attention: QK(t+1) into second score buffer, MFMAs 1-4 in the row-max tree, 5-6 in the first exp chunk, final two write the score registers directly afte
# speedup vs baseline: 1.0080x; 1.0012x over previous
; #define LAS __attribute__((address_space(3)))
; #define MFMA32(a, b, c) __builtin_amdgcn_mfma_f32_32x32x16_bf16((a), (b), (c), 0, 0, 0)
;     __device__ __forceinline__ void init(const void* A_, const void* B_, int lda_, int ldb_, int M, unsigned mask_, int G_, int c_) { A = (const char*)A_; B = (const char*)B_; lda = lda_; ldb = ldb_; nM = M / BM; mask = mask_; nN = __builtin_popcount(mask_); nwg = nM * nN; G = G_; c = c_; }
;     __device__ __forceinline__ void init(f32x4 (&acc)[2][2][4][2], const Unit& u, int wr, int wc, int fr, int fq) const { u32x4 old[2][4][2]; init_load(old, u, wr, wc, fr, fq); init_finish(acc, old); }
; template <int KS> DI void at_qk(f32x16& p0, f32x16& p1, LAS const unsigned char* Kt, int mapB, const bf16x8 (&qr)[8], float init, int r32, int hi) {
; #pragma unroll
;     for (int i = 0; i < 16; ++i) { p0[i] = init; p1[i] = init; }
;     bf16x8 kb[KS][2];
; #pragma unroll
;     for (int d0 = 0; d0 < KS; ++d0) { const int cb = mapB + (d0 * 16 + hi * 8) * 2;
;         kb[d0][0] = *(const LAS bf16x8*)(Kt + AT_KSWZ(r32, cb)); kb[d0][1] = *(const LAS bf16x8*)(Kt + AT_KSWZ(32 + r32, cb)); }
;     __builtin_amdgcn_sched_barrier(0);
; #pragma unroll
;     for (int d0 = 0; d0 < KS; ++d0) { p0 = MFMA32(kb[d0][0], qr[d0], p0); p1 = MFMA32(kb[d0][1], qr[d0], p1); }
; DI float at_softmax(f32x16& p0, f32x16& p1, float& m_run, bool first, bool nearb, LAS const float* tabp, int lane) {
;     if (nearb) {
; #pragma unroll
;         for (int i = 0; i < 16; ++i) { p0[i] += tabp[8 * (i >> 2) + (i & 3)]; p1[i] += tabp[32 + 8 * (i >> 2) + (i & 3)]; }
;     }
;     float mx = p0[0];
; #pragma unroll
;     for (int i = 1; i < 16; ++i) mx = fmaxf(mx, p0[i]);
; #pragma unroll
;     for (int i = 0; i < 16; ++i) mx = fmaxf(mx, p1[i]);
.LBB0_794:
	v_add_u32_e32 v0, s100, v161
	ds_read_b128 v[2:5], v0
	ds_read_b128 v[6:9], v0 offset:8192
	v_add_u32_e32 v0, s100, v162
	ds_read_b128 v[10:13], v0
	ds_read_b128 v[166:169], v0 offset:8192
	v_add_u32_e32 v0, s100, v163
	ds_read_b128 v[186:189], v0
	ds_read_b128 v[190:193], v0 offset:8192
	v_add_u32_e32 v0, s100, v164
	ds_read_b128 v[218:221], v0
	ds_read_b128 v[222:225], v0 offset:8192
	s_add_i32 s101, s48, 64
	s_cmp_le_u32 s101, s88
	s_cselect_b64 vcc, -1, 0
	v_cndmask_b32_e32 v15, 0, v158, vcc
	v_sub_f32_e32 v232, v15, v165
	v_mov_b32_e32 v233, v232
	v_mov_b32_e32 v234, v232
	v_mov_b32_e32 v235, v232
	v_mov_b32_e32 v236, v232
	v_mov_b32_e32 v237, v232
	v_mov_b32_e32 v238, v232
	v_mov_b32_e32 v239, v232
	v_mov_b32_e32 v240, v232
	v_mov_b32_e32 v241, v232
	v_mov_b32_e32 v242, v232
	v_mov_b32_e32 v243, v232
	v_mov_b32_e32 v244, v232
	v_mov_b32_e32 v245, v232
	v_mov_b32_e32 v246, v232
	v_mov_b32_e32 v247, v232
	v_max_f32_e32 v0, v113, v113
	v_max_f32_e32 v14, v112, v112
	v_max_f32_e32 v0, v14, v0
	v_max3_f32 v0, v0, v114, v115
	v_max3_f32 v0, v0, v116, v117
	s_waitcnt lgkmcnt(0)
	v_mfma_f32_32x32x16_bf16 v[202:217], v[2:5], v[128:131], v[232:247]
	v_max3_f32 v0, v0, v118, v119
	v_max3_f32 v0, v0, v120, v121
	v_max3_f32 v0, v0, v122, v123
	v_mfma_f32_32x32x16_bf16 v[232:247], v[6:9], v[128:131], v[232:247]
	v_max3_f32 v0, v0, v124, v125
	v_max3_f32 v0, v0, v126, v127
	v_max3_f32 v0, v0, v96, v97
	v_mfma_f32_32x32x16_bf16 v[202:217], v[10:13], v[132:135], v[202:217]
	v_max3_f32 v0, v0, v98, v99
	v_max3_f32 v0, v0, v100, v101
	v_max3_f32 v0, v0, v102, v103
	v_mfma_f32_32x32x16_bf16 v[232:247], v[166:169], v[132:135], v[232:247]
	v_max3_f32 v0, v0, v104, v105
	v_max3_f32 v0, v0, v106, v107
	v_max3_f32 v0, v0, v108, v109
	s_xor_b64 s[58:59], s[38:39], -1
	v_max3_f32 v2, v0, v110, v111
	s_and_b64 vcc, exec, s[58:59]
	s_cbranch_vccz .LBB0_796
	s_mov_b32 s58, 0x41000000
	v_cmp_ge_f32_e32 vcc, s58, v2
	s_cmp_lg_u64 vcc, exec
	s_cselect_b64 s[58:59], -1, 0
	s_cbranch_execz .LBB0_797
	s_branch .LBB0_798

; #define MFMA32(a, b, c) __builtin_amdgcn_mfma_f32_32x32x16_bf16((a), (b), (c), 0, 0, 0)
; template <int OFF> DI s16x4 at_tr_read(int vb) { s16x4 r; asm volatile("ds_read_b64_tr_b16 %0, %1 offset:%2" : "=&v"(r) : "v"(vb), "i"(OFF) : "memory"); return r; }
; DI unsigned at_cvtpk(float lo, float hi) { unsigned r; asm volatile("v_cvt_pk_bf16_f32 %0, %1, %2" : "=v"(r) : "v"(lo), "v"(hi)); return r; }
; DI float at_softmax(f32x16& p0, f32x16& p1, float& m_run, bool first, bool nearb, LAS const float* tabp, int lane) {
;     ...
;     for (int i = 0; i < 16; ++i) p0[i] = __builtin_amdgcn_exp2f(p0[i]);
; #pragma unroll
;     for (int i = 0; i < 16; ++i) p1[i] = __builtin_amdgcn_exp2f(p1[i]);
;     return alpha;
; }
; DI bf16x8 at_pack(const f32x16& p, int s8) {
;     u32x4 w; w.x = at_cvtpk(p[s8], p[s8 + 1]); w.y = at_cvtpk(p[s8 + 2], p[s8 + 3]); w.z = at_cvtpk(p[s8 + 4], p[s8 + 5]); w.w = at_cvtpk(p[s8 + 6], p[s8 + 7]);
;     return __builtin_bit_cast(bf16x8, w);
; }
; template <int D0> DI void at_pv_block(f32x16 (&o)[4], int vb, const bf16x8 (&pf)[4]) {
;     const s16x4 l0 = at_tr_read<D0 * 512 + 0 * 4096>(vb), h0 = at_tr_read<D0 * 512 + 0 * 4096 + 2048>(vb), l1 = at_tr_read<D0 * 512 + 1 * 4096>(vb), h1 = at_tr_read<D0 * 512 + 1 * 4096 + 2048>(vb);
;     const s16x4 l2 = at_tr_read<D0 * 512 + 2 * 4096>(vb), h2 = at_tr_read<D0 * 512 + 2 * 4096 + 2048>(vb), l3 = at_tr_read<D0 * 512 + 3 * 4096>(vb), h3 = at_tr_read<D0 * 512 + 3 * 4096 + 2048>(vb);
;     asm volatile("s_waitcnt lgkmcnt(0)" ::: "memory"); __builtin_amdgcn_sched_barrier(0);
;     ...
;     o[D0] = MFMA32(AT_PK(l0, h0), pf[0], o[D0]); o[D0] = MFMA32(AT_PK(l1, h1), pf[1], o[D0]); o[D0] = MFMA32(AT_PK(l2, h2), pf[2], o[D0]); o[D0] = MFMA32(AT_PK(l3, h3), pf[3], o[D0]);
; DI void attn_unit_diff(const Ctx& C, int l, int b, int h, int j) {
;     ...
;             pf[0] = at_pack(p0, 0); pf[1] = at_pack(p0, 8); pf[2] = at_pack(p1, 0); pf[3] = at_pack(p1, 8);
;             ol = MFMA32(ones, pf[0], ol); ol = MFMA32(ones, pf[1], ol); ol = MFMA32(ones, pf[2], ol); ol = MFMA32(ones, pf[3], ol);
;             at_pv_block<0>(o, vb, pf); at_pv_block<1>(o, vb, pf); at_pv_block<2>(o, vb, pf); at_pv_block<3>(o, vb, pf);
.LBB0_801:
	v_subrev_u32_e32 v87, s57, v160
	v_add_u32_e32 v87, s49, v87
	ds_read_b64_tr_b16 v[170:171], v87 offset:0x0
	ds_read_b64_tr_b16 v[172:173], v87 offset:0x800
	ds_read_b64_tr_b16 v[174:175], v87 offset:0x200
	ds_read_b64_tr_b16 v[176:177], v87 offset:0xa00
	ds_read_b64_tr_b16 v[178:179], v87 offset:0x400
	ds_read_b64_tr_b16 v[180:181], v87 offset:0xc00
	ds_read_b64_tr_b16 v[182:183], v87 offset:0x600
	ds_read_b64_tr_b16 v[184:185], v87 offset:0xe00
	v_exp_f32_e32 v112, v112
	v_exp_f32_e32 v113, v113
	v_mfma_f32_32x32x16_bf16 v[202:217], v[186:189], v[136:139], v[202:217]
	v_exp_f32_e32 v114, v114
	v_exp_f32_e32 v115, v115
	v_mfma_f32_32x32x16_bf16 v[232:247], v[190:193], v[136:139], v[232:247]
	v_exp_f32_e32 v116, v116
	v_exp_f32_e32 v117, v117
	v_exp_f32_e32 v118, v118
	v_exp_f32_e32 v119, v119
	v_cvt_pk_bf16_f32 v2, v112, v113
	v_cvt_pk_bf16_f32 v3, v114, v115
	v_cvt_pk_bf16_f32 v4, v116, v117
	v_cvt_pk_bf16_f32 v5, v118, v119
	v_add_f32_e32 v81, v112, v113
	v_add_f32_e32 v82, v114, v115
	v_add_f32_e32 v83, v116, v117
	v_add_f32_e32 v84, v118, v119
	v_add_f32_e32 v81, v81, v82
	v_add_f32_e32 v83, v83, v84
	v_add_f32_e32 v81, v81, v83
	v_add_f32_e32 v80, v80, v81
	s_waitcnt lgkmcnt(0)
	ds_read_b64_tr_b16 v[112:113], v87 offset:0x1000
	ds_read_b64_tr_b16 v[114:115], v87 offset:0x1800
	ds_read_b64_tr_b16 v[116:117], v87 offset:0x1200
	ds_read_b64_tr_b16 v[118:119], v87 offset:0x1a00
	ds_read_b64_tr_b16 v[88:89], v87 offset:0x1400
	ds_read_b64_tr_b16 v[90:91], v87 offset:0x1c00
	ds_read_b64_tr_b16 v[92:93], v87 offset:0x1600
	ds_read_b64_tr_b16 v[94:95], v87 offset:0x1e00
	v_mfma_f32_32x32x16_bf16 v[64:79], v[170:173], v[2:5], v[64:79]
	v_exp_f32_e32 v120, v120
	v_exp_f32_e32 v121, v121
	v_mfma_f32_32x32x16_bf16 v[48:63], v[174:177], v[2:5], v[48:63]
	v_exp_f32_e32 v122, v122
	v_exp_f32_e32 v123, v123
	v_mfma_f32_32x32x16_bf16 v[32:47], v[178:181], v[2:5], v[32:47]
	v_exp_f32_e32 v124, v124
	v_exp_f32_e32 v125, v125
	v_mfma_f32_32x32x16_bf16 v[16:31], v[182:185], v[2:5], v[16:31]
	v_exp_f32_e32 v126, v126
	v_exp_f32_e32 v127, v127
	v_cvt_pk_bf16_f32 v6, v120, v121
	v_cvt_pk_bf16_f32 v7, v122, v123
	v_cvt_pk_bf16_f32 v8, v124, v125
	v_cvt_pk_bf16_f32 v9, v126, v127
	v_add_f32_e32 v81, v120, v121
	v_add_f32_e32 v82, v122, v123
	v_add_f32_e32 v83, v124, v125
	v_add_f32_e32 v84, v126, v127
	v_add_f32_e32 v81, v81, v82
	v_add_f32_e32 v83, v83, v84
	v_add_f32_e32 v81, v81, v83
	v_add_f32_e32 v80, v80, v81
	s_waitcnt lgkmcnt(0)
	ds_read_b64_tr_b16 v[170:171], v87 offset:0x2000
	ds_read_b64_tr_b16 v[172:173], v87 offset:0x2800
	ds_read_b64_tr_b16 v[174:175], v87 offset:0x2200
	ds_read_b64_tr_b16 v[176:177], v87 offset:0x2a00
	ds_read_b64_tr_b16 v[178:179], v87 offset:0x2400
	ds_read_b64_tr_b16 v[180:181], v87 offset:0x2c00
	ds_read_b64_tr_b16 v[182:183], v87 offset:0x2600
	ds_read_b64_tr_b16 v[184:185], v87 offset:0x2e00
	v_mfma_f32_32x32x16_bf16 v[64:79], v[112:115], v[6:9], v[64:79]
	v_exp_f32_e32 v96, v96
	v_exp_f32_e32 v97, v97
	v_mfma_f32_32x32x16_bf16 v[48:63], v[116:119], v[6:9], v[48:63]
	v_exp_f32_e32 v98, v98
	v_exp_f32_e32 v99, v99
	v_mfma_f32_32x32x16_bf16 v[32:47], v[88:91], v[6:9], v[32:47]
	v_exp_f32_e32 v100, v100
	v_exp_f32_e32 v101, v101
	v_mfma_f32_32x32x16_bf16 v[16:31], v[92:95], v[6:9], v[16:31]
	v_exp_f32_e32 v102, v102
	v_exp_f32_e32 v103, v103
	v_cvt_pk_bf16_f32 v10, v96, v97
	v_cvt_pk_bf16_f32 v11, v98, v99
	v_cvt_pk_bf16_f32 v12, v100, v101
	v_cvt_pk_bf16_f32 v13, v102, v103
	v_add_f32_e32 v81, v96, v97
	v_add_f32_e32 v82, v98, v99
	v_add_f32_e32 v83, v100, v101
	v_add_f32_e32 v84, v102, v103
	v_add_f32_e32 v81, v81, v82
	v_add_f32_e32 v83, v83, v84
	v_add_f32_e32 v81, v81, v83
	v_add_f32_e32 v80, v80, v81
	s_waitcnt lgkmcnt(0)
	ds_read_b64_tr_b16 v[112:113], v87 offset:0x3000
	ds_read_b64_tr_b16 v[114:115], v87 offset:0x3800
	ds_read_b64_tr_b16 v[116:117], v87 offset:0x3200
	ds_read_b64_tr_b16 v[118:119], v87 offset:0x3a00
	ds_read_b64_tr_b16 v[88:89], v87 offset:0x3400
	ds_read_b64_tr_b16 v[90:91], v87 offset:0x3c00
	ds_read_b64_tr_b16 v[92:93], v87 offset:0x3600
	ds_read_b64_tr_b16 v[94:95], v87 offset:0x3e00
	v_mfma_f32_32x32x16_bf16 v[64:79], v[170:173], v[10:13], v[64:79]
	v_exp_f32_e32 v104, v104
	v_exp_f32_e32 v105, v105
	v_mfma_f32_32x32x16_bf16 v[48:63], v[174:177], v[10:13], v[48:63]
	v_exp_f32_e32 v106, v106
	v_exp_f32_e32 v107, v107
	v_mfma_f32_32x32x16_bf16 v[32:47], v[178:181], v[10:13], v[32:47]
	v_exp_f32_e32 v108, v108
	v_exp_f32_e32 v109, v109
	v_mfma_f32_32x32x16_bf16 v[16:31], v[182:185], v[10:13], v[16:31]
	v_exp_f32_e32 v110, v110
	v_exp_f32_e32 v111, v111
	v_cvt_pk_bf16_f32 v166, v104, v105
	v_cvt_pk_bf16_f32 v167, v106, v107
	v_cvt_pk_bf16_f32 v168, v108, v109
	v_cvt_pk_bf16_f32 v169, v110, v111
	v_add_f32_e32 v81, v104, v105
	v_add_f32_e32 v82, v106, v107
	v_add_f32_e32 v83, v108, v109
	v_add_f32_e32 v84, v110, v111
	v_add_f32_e32 v81, v81, v82
	v_add_f32_e32 v83, v83, v84
	v_add_f32_e32 v81, v81, v83
	v_add_f32_e32 v80, v80, v81
	s_waitcnt lgkmcnt(0)
	v_mfma_f32_32x32x16_bf16 v[64:79], v[112:115], v[166:169], v[64:79]
	v_mfma_f32_32x32x16_bf16 v[48:63], v[116:119], v[166:169], v[48:63]
	v_mfma_f32_32x32x16_bf16 v[32:47], v[88:91], v[166:169], v[32:47]
	v_mfma_f32_32x32x16_bf16 v[16:31], v[92:95], v[166:169], v[16:31]
	v_mfma_f32_32x32x16_bf16 v[112:127], v[218:221], v[140:143], v[202:217]
	v_mfma_f32_32x32x16_bf16 v[96:111], v[222:225], v[140:143], v[232:247]
	s_mov_b64 s[38:39], 0
	s_mov_b64 s[58:59], -1
	s_and_b64 vcc, exec, s[40:41]
	s_cbranch_vccz .LBB0_790

; #define LAS __attribute__((address_space(3)))
; #define MFMA32(a, b, c) __builtin_amdgcn_mfma_f32_32x32x16_bf16((a), (b), (c), 0, 0, 0)
;     __device__ __forceinline__ void init(const void* A_, const void* B_, int lda_, int ldb_, int M, unsigned mask_, int G_, int c_) { A = (const char*)A_; B = (const char*)B_; lda = lda_; ldb = ldb_; nM = M / BM; mask = mask_; nN = __builtin_popcount(mask_); nwg = nM * nN; G = G_; c = c_; }
;     __device__ __forceinline__ void init(f32x4 (&acc)[2][2][4][2], const Unit& u, int wr, int wc, int fr, int fq) const { u32x4 old[2][4][2]; init_load(old, u, wr, wc, fr, fq); init_finish(acc, old); }
; template <int KS> DI void at_qk(f32x16& p0, f32x16& p1, LAS const unsigned char* Kt, int mapB, const bf16x8 (&qr)[8], float init, int r32, int hi) {
; #pragma unroll
;     for (int i = 0; i < 16; ++i) { p0[i] = init; p1[i] = init; }
;     bf16x8 kb[KS][2];
; #pragma unroll
;     for (int d0 = 0; d0 < KS; ++d0) { const int cb = mapB + (d0 * 16 + hi * 8) * 2;
;         kb[d0][0] = *(const LAS bf16x8*)(Kt + AT_KSWZ(r32, cb)); kb[d0][1] = *(const LAS bf16x8*)(Kt + AT_KSWZ(32 + r32, cb)); }
;     __builtin_amdgcn_sched_barrier(0);
; #pragma unroll
;     for (int d0 = 0; d0 < KS; ++d0) { p0 = MFMA32(kb[d0][0], qr[d0], p0); p1 = MFMA32(kb[d0][1], qr[d0], p1); }
; DI float at_softmax(f32x16& p0, f32x16& p1, float& m_run, bool first, bool nearb, LAS const float* tabp, int lane) {
;     if (nearb) {
; #pragma unroll
;         for (int i = 0; i < 16; ++i) { p0[i] += tabp[8 * (i >> 2) + (i & 3)]; p1[i] += tabp[32 + 8 * (i >> 2) + (i & 3)]; }
;     }
;     float mx = p0[0];
; #pragma unroll
;     for (int i = 1; i < 16; ++i) mx = fmaxf(mx, p0[i]);
; #pragma unroll
;     for (int i = 0; i < 16; ++i) mx = fmaxf(mx, p1[i]);
.LBB0_837:
	v_add_u32_e32 v0, s100, v161
	ds_read_b128 v[2:5], v0
	ds_read_b128 v[6:9], v0 offset:8192
	v_add_u32_e32 v0, s100, v162
	ds_read_b128 v[10:13], v0
	ds_read_b128 v[166:169], v0 offset:8192
	v_add_u32_e32 v0, s100, v163
	ds_read_b128 v[186:189], v0
	ds_read_b128 v[190:193], v0 offset:8192
	v_add_u32_e32 v0, s100, v164
	ds_read_b128 v[218:221], v0
	ds_read_b128 v[222:225], v0 offset:8192
	s_add_i32 s101, s28, 64
	s_cmp_le_i32 s101, s16
	s_cselect_b64 vcc, -1, 0
	v_cndmask_b32_e32 v15, 0, v158, vcc
	v_sub_f32_e32 v232, v15, v165
	v_mov_b32_e32 v233, v232
	v_mov_b32_e32 v234, v232
	v_mov_b32_e32 v235, v232
	v_mov_b32_e32 v236, v232
	v_mov_b32_e32 v237, v232
	v_mov_b32_e32 v238, v232
	v_mov_b32_e32 v239, v232
	v_mov_b32_e32 v240, v232
	v_mov_b32_e32 v241, v232
	v_mov_b32_e32 v242, v232
	v_mov_b32_e32 v243, v232
	v_mov_b32_e32 v244, v232
	v_mov_b32_e32 v245, v232
	v_mov_b32_e32 v246, v232
	v_mov_b32_e32 v247, v232
	v_max_f32_e32 v0, v113, v113
	v_max_f32_e32 v14, v112, v112
	v_max_f32_e32 v0, v14, v0
	v_max3_f32 v0, v0, v114, v115
	v_max3_f32 v0, v0, v116, v117
	s_waitcnt lgkmcnt(0)
	v_mfma_f32_32x32x16_bf16 v[202:217], v[2:5], v[128:131], v[232:247]
	v_max3_f32 v0, v0, v118, v119
	v_max3_f32 v0, v0, v120, v121
	v_max3_f32 v0, v0, v122, v123
	v_mfma_f32_32x32x16_bf16 v[232:247], v[6:9], v[128:131], v[232:247]
	v_max3_f32 v0, v0, v124, v125
	v_max3_f32 v0, v0, v126, v127
	v_max3_f32 v0, v0, v96, v97
	v_mfma_f32_32x32x16_bf16 v[202:217], v[10:13], v[132:135], v[202:217]
	v_max3_f32 v0, v0, v98, v99
	v_max3_f32 v0, v0, v100, v101
	v_max3_f32 v0, v0, v102, v103
	v_mfma_f32_32x32x16_bf16 v[232:247], v[166:169], v[132:135], v[232:247]
	v_max3_f32 v0, v0, v104, v105
	v_max3_f32 v0, v0, v106, v107
	v_max3_f32 v0, v0, v108, v109
	s_xor_b64 s[58:59], s[42:43], -1
	v_max3_f32 v2, v0, v110, v111
	s_and_b64 vcc, exec, s[58:59]
	s_cbranch_vccz .LBB0_839
	s_mov_b32 s49, 0x41000000
	v_cmp_ge_f32_e32 vcc, s49, v2
	s_cmp_lg_u64 vcc, exec
	s_cselect_b64 s[58:59], -1, 0
	s_cbranch_execz .LBB0_840
	s_branch .LBB0_841

; #define LAS __attribute__((address_space(3)))
; DI float max_x32(float v, int lane) { return fmaxf(v, bpx(v, lane, 32)); }
; #define MFMA32(a, b, c) __builtin_amdgcn_mfma_f32_32x32x16_bf16((a), (b), (c), 0, 0, 0)
; DI unsigned at_cvtpk(float lo, float hi) { unsigned r; asm volatile("v_cvt_pk_bf16_f32 %0, %1, %2" : "=v"(r) : "v"(lo), "v"(hi)); return r; }
; DI float at_softmax(f32x16& p0, f32x16& p1, float& m_run, bool first, bool nearb, LAS const float* tabp, int lane) {
;     if (nearb) {
; #pragma unroll
;         for (int i = 0; i < 16; ++i) { p0[i] += tabp[8 * (i >> 2) + (i & 3)]; p1[i] += tabp[32 + 8 * (i >> 2) + (i & 3)]; }
;     }
;     float mx = p0[0];
; #pragma unroll
;     for (int i = 1; i < 16; ++i) mx = fmaxf(mx, p0[i]);
; #pragma unroll
;     for (int i = 0; i < 16; ++i) mx = fmaxf(mx, p1[i]);
;     float alpha = 1.f;
;     if (first || !__all(mx <= AT_THR)) {
;         mx = max_x32(mx, lane);
;         const float dl = first ? mx : fmaxf(mx, 0.f);
;         alpha = first ? 1.f : __builtin_amdgcn_exp2f(-dl); m_run += dl;
; #pragma unroll
;         for (int i = 0; i < 16; ++i) { p0[i] -= dl; p1[i] -= dl; }
;     }
; #pragma unroll
;     for (int i = 0; i < 16; ++i) p0[i] = __builtin_amdgcn_exp2f(p0[i]);
; #pragma unroll
;     for (int i = 0; i < 16; ++i) p1[i] = __builtin_amdgcn_exp2f(p1[i]);
;     return alpha;
; }
; DI bf16x8 at_pack(const f32x16& p, int s8) {
;     u32x4 w; w.x = at_cvtpk(p[s8], p[s8 + 1]); w.y = at_cvtpk(p[s8 + 2], p[s8 + 3]); w.z = at_cvtpk(p[s8 + 4], p[s8 + 5]); w.w = at_cvtpk(p[s8 + 6], p[s8 + 7]);
;     return __builtin_bit_cast(bf16x8, w);
; }
; template <int D0> DI void at_pv_block(f32x16 (&o)[4], int vb, const bf16x8 (&pf)[4]) {
;     const s16x4 l0 = at_tr_read<D0 * 512 + 0 * 4096>(vb), h0 = at_tr_read<D0 * 512 + 0 * 4096 + 2048>(vb), l1 = at_tr_read<D0 * 512 + 1 * 4096>(vb), h1 = at_tr_read<D0 * 512 + 1 * 4096 + 2048>(vb);
;     const s16x4 l2 = at_tr_read<D0 * 512 + 2 * 4096>(vb), h2 = at_tr_read<D0 * 512 + 2 * 4096 + 2048>(vb), l3 = at_tr_read<D0 * 512 + 3 * 4096>(vb), h3 = at_tr_read<D0 * 512 + 3 * 4096 + 2048>(vb);
;     asm volatile("s_waitcnt lgkmcnt(0)" ::: "memory"); __builtin_amdgcn_sched_barrier(0);
;     ...
;     o[D0] = MFMA32(AT_PK(l0, h0), pf[0], o[D0]); o[D0] = MFMA32(AT_PK(l1, h1), pf[1], o[D0]); o[D0] = MFMA32(AT_PK(l2, h2), pf[2], o[D0]); o[D0] = MFMA32(AT_PK(l3, h3), pf[3], o[D0]);
.LBB0_844:
	v_subrev_u32_e32 v87, s48, v160
	v_add_u32_e32 v87, s31, v87
	ds_read_b64_tr_b16 v[170:171], v87 offset:0x0
	ds_read_b64_tr_b16 v[172:173], v87 offset:0x800
	ds_read_b64_tr_b16 v[174:175], v87 offset:0x200
	ds_read_b64_tr_b16 v[176:177], v87 offset:0xa00
	ds_read_b64_tr_b16 v[178:179], v87 offset:0x400
	ds_read_b64_tr_b16 v[180:181], v87 offset:0xc00
	ds_read_b64_tr_b16 v[182:183], v87 offset:0x600
	ds_read_b64_tr_b16 v[184:185], v87 offset:0xe00
	v_exp_f32_e32 v112, v112
	v_exp_f32_e32 v113, v113
	v_mfma_f32_32x32x16_bf16 v[202:217], v[186:189], v[136:139], v[202:217]
	v_exp_f32_e32 v114, v114
	v_exp_f32_e32 v115, v115
	v_mfma_f32_32x32x16_bf16 v[232:247], v[190:193], v[136:139], v[232:247]
	v_exp_f32_e32 v116, v116
	v_exp_f32_e32 v117, v117
	v_exp_f32_e32 v118, v118
	v_exp_f32_e32 v119, v119
	v_cvt_pk_bf16_f32 v2, v112, v113
	v_cvt_pk_bf16_f32 v3, v114, v115
	v_cvt_pk_bf16_f32 v4, v116, v117
	v_cvt_pk_bf16_f32 v5, v118, v119
	v_add_f32_e32 v81, v112, v113
	v_add_f32_e32 v82, v114, v115
	v_add_f32_e32 v83, v116, v117
	v_add_f32_e32 v84, v118, v119
	v_add_f32_e32 v81, v81, v82
	v_add_f32_e32 v83, v83, v84
	v_add_f32_e32 v81, v81, v83
	v_add_f32_e32 v80, v80, v81
	s_waitcnt lgkmcnt(0)
	ds_read_b64_tr_b16 v[112:113], v87 offset:0x1000
	ds_read_b64_tr_b16 v[114:115], v87 offset:0x1800
	ds_read_b64_tr_b16 v[116:117], v87 offset:0x1200
	ds_read_b64_tr_b16 v[118:119], v87 offset:0x1a00
	ds_read_b64_tr_b16 v[88:89], v87 offset:0x1400
	ds_read_b64_tr_b16 v[90:91], v87 offset:0x1c00
	ds_read_b64_tr_b16 v[92:93], v87 offset:0x1600
	ds_read_b64_tr_b16 v[94:95], v87 offset:0x1e00
	v_mfma_f32_32x32x16_bf16 v[64:79], v[170:173], v[2:5], v[64:79]
	v_exp_f32_e32 v120, v120
	v_exp_f32_e32 v121, v121
	v_mfma_f32_32x32x16_bf16 v[48:63], v[174:177], v[2:5], v[48:63]
	v_exp_f32_e32 v122, v122
	v_exp_f32_e32 v123, v123
	v_mfma_f32_32x32x16_bf16 v[32:47], v[178:181], v[2:5], v[32:47]
	v_exp_f32_e32 v124, v124
	v_exp_f32_e32 v125, v125
	v_mfma_f32_32x32x16_bf16 v[16:31], v[182:185], v[2:5], v[16:31]
	v_exp_f32_e32 v126, v126
	v_exp_f32_e32 v127, v127
	v_cvt_pk_bf16_f32 v6, v120, v121
	v_cvt_pk_bf16_f32 v7, v122, v123
	v_cvt_pk_bf16_f32 v8, v124, v125
	v_cvt_pk_bf16_f32 v9, v126, v127
	v_add_f32_e32 v81, v120, v121
	v_add_f32_e32 v82, v122, v123
	v_add_f32_e32 v83, v124, v125
	v_add_f32_e32 v84, v126, v127
	v_add_f32_e32 v81, v81, v82
	v_add_f32_e32 v83, v83, v84
	v_add_f32_e32 v81, v81, v83
	v_add_f32_e32 v80, v80, v81
	s_waitcnt lgkmcnt(0)
	ds_read_b64_tr_b16 v[170:171], v87 offset:0x2000
	ds_read_b64_tr_b16 v[172:173], v87 offset:0x2800
	ds_read_b64_tr_b16 v[174:175], v87 offset:0x2200
	ds_read_b64_tr_b16 v[176:177], v87 offset:0x2a00
	ds_read_b64_tr_b16 v[178:179], v87 offset:0x2400
	ds_read_b64_tr_b16 v[180:181], v87 offset:0x2c00
	ds_read_b64_tr_b16 v[182:183], v87 offset:0x2600
	ds_read_b64_tr_b16 v[184:185], v87 offset:0x2e00
	v_mfma_f32_32x32x16_bf16 v[64:79], v[112:115], v[6:9], v[64:79]
	v_exp_f32_e32 v96, v96
	v_exp_f32_e32 v97, v97
	v_mfma_f32_32x32x16_bf16 v[48:63], v[116:119], v[6:9], v[48:63]
	v_exp_f32_e32 v98, v98
	v_exp_f32_e32 v99, v99
	v_mfma_f32_32x32x16_bf16 v[32:47], v[88:91], v[6:9], v[32:47]
	v_exp_f32_e32 v100, v100
	v_exp_f32_e32 v101, v101
	v_mfma_f32_32x32x16_bf16 v[16:31], v[92:95], v[6:9], v[16:31]
	v_exp_f32_e32 v102, v102
	v_exp_f32_e32 v103, v103
	v_cvt_pk_bf16_f32 v10, v96, v97
	v_cvt_pk_bf16_f32 v11, v98, v99
	v_cvt_pk_bf16_f32 v12, v100, v101
	v_cvt_pk_bf16_f32 v13, v102, v103
	v_add_f32_e32 v81, v96, v97
	v_add_f32_e32 v82, v98, v99
	v_add_f32_e32 v83, v100, v101
	v_add_f32_e32 v84, v102, v103
	v_add_f32_e32 v81, v81, v82
	v_add_f32_e32 v83, v83, v84
	v_add_f32_e32 v81, v81, v83
	v_add_f32_e32 v80, v80, v81
	s_waitcnt lgkmcnt(0)
	ds_read_b64_tr_b16 v[112:113], v87 offset:0x3000
	ds_read_b64_tr_b16 v[114:115], v87 offset:0x3800
	ds_read_b64_tr_b16 v[116:117], v87 offset:0x3200
	ds_read_b64_tr_b16 v[118:119], v87 offset:0x3a00
	ds_read_b64_tr_b16 v[88:89], v87 offset:0x3400
	ds_read_b64_tr_b16 v[90:91], v87 offset:0x3c00
	ds_read_b64_tr_b16 v[92:93], v87 offset:0x3600
	ds_read_b64_tr_b16 v[94:95], v87 offset:0x3e00
	v_mfma_f32_32x32x16_bf16 v[64:79], v[170:173], v[10:13], v[64:79]
	v_exp_f32_e32 v104, v104
	v_exp_f32_e32 v105, v105
	v_mfma_f32_32x32x16_bf16 v[48:63], v[174:177], v[10:13], v[48:63]
	v_exp_f32_e32 v106, v106
	v_exp_f32_e32 v107, v107
	v_mfma_f32_32x32x16_bf16 v[32:47], v[178:181], v[10:13], v[32:47]
	v_exp_f32_e32 v108, v108
	v_exp_f32_e32 v109, v109
	v_mfma_f32_32x32x16_bf16 v[16:31], v[182:185], v[10:13], v[16:31]
	v_exp_f32_e32 v110, v110
	v_exp_f32_e32 v111, v111
	v_cvt_pk_bf16_f32 v166, v104, v105
	v_cvt_pk_bf16_f32 v167, v106, v107
	v_cvt_pk_bf16_f32 v168, v108, v109
	v_cvt_pk_bf16_f32 v169, v110, v111
	v_add_f32_e32 v81, v104, v105
	v_add_f32_e32 v82, v106, v107
	v_add_f32_e32 v83, v108, v109
	v_add_f32_e32 v84, v110, v111
	v_add_f32_e32 v81, v81, v82
	v_add_f32_e32 v83, v83, v84
	v_add_f32_e32 v81, v81, v83
	v_add_f32_e32 v80, v80, v81
	s_waitcnt lgkmcnt(0)
	v_mfma_f32_32x32x16_bf16 v[64:79], v[112:115], v[166:169], v[64:79]
	v_mfma_f32_32x32x16_bf16 v[48:63], v[116:119], v[166:169], v[48:63]
	v_mfma_f32_32x32x16_bf16 v[32:47], v[88:91], v[166:169], v[32:47]
	v_mfma_f32_32x32x16_bf16 v[16:31], v[92:95], v[166:169], v[16:31]
	v_mfma_f32_32x32x16_bf16 v[112:127], v[218:221], v[140:143], v[202:217]
	v_mfma_f32_32x32x16_bf16 v[96:111], v[222:225], v[140:143], v[232:247]
	s_mov_b64 s[42:43], 0
	s_mov_b64 s[58:59], -1
	s_and_b64 vcc, exec, s[76:77]
	s_cbranch_vccz .LBB0_833
